# speedup vs baseline: 1.0330x; 1.0007x over previous
.Ltg1_go:
	s_nop 1
	v_accvgpr_read_b32 v0, a0
	v_accvgpr_read_b32 v2, a1
	v_accvgpr_read_b32 v1, a2
	v_accvgpr_read_b32 v3, a3
	v_cvt_pk_f16_f32 v1, v1, v3
	v_cvt_pk_f16_f32 v0, v0, v2
	v_add_u32_e32 v182, v111, v207
	v_accvgpr_read_b32 v2, a4
	v_accvgpr_read_b32 v6, a5
	v_accvgpr_read_b32 v3, a6
	v_accvgpr_read_b32 v7, a7
	v_cvt_pk_f16_f32 v3, v3, v7
	v_cvt_pk_f16_f32 v2, v2, v6
	ds_write2_b64 v248, v[0:1], v[2:3] offset0:80 offset1:96
	s_waitcnt lgkmcnt(0)
	s_barrier
	ds_read_b128 v[0:3], v182 offset:12800
	ds_read_b128 v[6:9], v182 offset:12864
	ds_read_b128 v[10:13], v182 offset:12928
	ds_read_b128 v[14:17], v182 offset:12992
	ds_read_b128 v[18:21], v182 offset:13056
	ds_read_b128 v[22:25], v182 offset:13120
	ds_read2st64_b32 v[42:43], v242 offset0:84 offset1:116
	ds_read_b128 v[38:41], v225 offset:33792
	ds_read_b128 v[26:29], v225 offset:33856
	ds_read_b128 v[30:33], v225 offset:33920
	v_or_b32_e32 v36, v110, v227
	v_or_b32_e32 v34, v110, v226
	ds_read2st64_b32 v[44:45], v36 offset0:84 offset1:116
	v_or_b32_e32 v36, v110, v228
	ds_read2st64_b32 v[34:35], v34 offset0:84 offset1:116
	ds_read2st64_b32 v[36:37], v36 offset0:84 offset1:116
	s_waitcnt lgkmcnt(12)
	v_mfma_f32_16x16x32_f16 a[0:3], v[0:3], a[56:59], 0
	s_waitcnt lgkmcnt(11)
	v_mfma_f32_16x16x32_f16 a[0:3], v[6:9], a[60:63], a[0:3]
	s_waitcnt lgkmcnt(10)
	v_mfma_f32_16x16x32_f16 a[0:3], v[10:13], a[64:67], a[0:3]
	s_waitcnt lgkmcnt(9)
	v_mfma_f32_16x16x32_f16 a[0:3], v[14:17], a[68:71], a[0:3]
	s_waitcnt lgkmcnt(8)
	v_mfma_f32_16x16x32_f16 a[0:3], v[18:21], a[72:75], a[0:3]
	s_waitcnt lgkmcnt(7)
	v_mfma_f32_16x16x32_f16 a[0:3], v[22:25], a[76:79], a[0:3]
	s_waitcnt vmcnt(0) lgkmcnt(3)
	v_mul_f32_e32 v0, v191, v26
	v_mul_f32_e32 v1, v191, v27
	v_mul_f32_e32 v2, v191, v28
	v_mul_f32_e32 v3, v191, v29
	v_fma_f32 v0, v190, v38, v0
	v_fma_f32 v1, v190, v39, v1
	v_fma_f32 v2, v190, v40, v2
	v_fma_f32 v3, v190, v41, v3
	v_mul_f32_e32 v6, v192, v30
	v_mul_f32_e32 v7, v192, v31
	v_mul_f32_e32 v8, v192, v32
	v_mul_f32_e32 v9, v192, v33
	v_add_f32_e32 v46, v0, v6
	v_add_f32_e32 v47, v1, v7
	v_add_f32_e32 v48, v2, v8
	v_add_f32_e32 v49, v3, v9
	v_accvgpr_read_b32 v0, a0
	v_accvgpr_read_b32 v1, a1
	v_accvgpr_read_b32 v2, a2
	v_accvgpr_read_b32 v3, a3
	v_add_f32_e32 v0, v186, v0
	v_add_f32_e32 v1, v186, v1
	v_add_f32_e32 v2, v186, v2
	v_add_f32_e32 v3, v186, v3
	v_add_f32_e32 v0, v46, v0
	v_add_f32_e32 v1, v47, v1
	v_add_f32_e32 v2, v48, v2
	v_add_f32_e32 v3, v49, v3
	v_mul_f32_e32 v0, 0x4038aa3b, v0
	v_mul_f32_e32 v1, 0x4038aa3b, v1
	v_mul_f32_e32 v2, 0x4038aa3b, v2
	v_mul_f32_e32 v3, 0x4038aa3b, v3
	v_exp_f32_e32 v0, v0
	v_exp_f32_e32 v1, v1
	v_exp_f32_e32 v2, v2
	v_exp_f32_e32 v3, v3
	v_add_f32_e32 v0, 1.0, v0
	v_add_f32_e32 v1, 1.0, v1
	v_add_f32_e32 v2, 1.0, v2
	v_add_f32_e32 v3, 1.0, v3
	v_rcp_f32_e32 v0, v0
	v_rcp_f32_e32 v1, v1
	v_rcp_f32_e32 v2, v2
	v_rcp_f32_e32 v3, v3
	s_waitcnt lgkmcnt(0)
	s_and_b64 vcc, exec, s[16:17]
	v_sub_f32_e32 v6, 1.0, v43
	v_sub_f32_e32 v7, 1.0, v35
	v_sub_f32_e32 v12, 1.0, v45
	v_sub_f32_e32 v13, 1.0, v37
	v_fma_f32 v0, -v0, 2.0, 1.0
	v_fma_f32 v1, -v1, 2.0, 1.0
	v_fma_f32 v2, -v2, 2.0, 1.0
	v_fma_f32 v3, -v3, 2.0, 1.0
	v_mul_f32_e32 v0, v6, v0
	v_mul_f32_e32 v1, v7, v1
	v_mul_f32_e32 v2, v12, v2
	v_mul_f32_e32 v3, v13, v3
	v_fma_f32 v8, v42, v43, v0
	v_fma_f32 v9, v34, v35, v1
	v_fma_f32 v10, v44, v45, v2
	v_fma_f32 v11, v36, v37, v3
	v_cvt_pk_f16_f32 v6, v8, v9
	v_cvt_pk_f16_f32 v7, v10, v11
	v_mov_b32_e32 v2, v6
	v_or_b32_e32 v3, s64, v7
	s_cbranch_vccnz .LBB1_125
	s_mov_b64 s[36:37], 0
	global_store_dwordx2 v[178:179], v[2:3], off
	s_or_b32 s70, s40, 2
	s_and_saveexec_b64 s[68:69], s[12:13]
	v_mov_b32_e32 v0, s70
	global_store_dword v[174:175], v0, off
	s_mov_b64 exec, s[68:69]
